# nt on fp8 conversion stores in mLSTM phase
# speedup vs baseline: 1.0042x; 1.0042x over previous
.LBB0_556:
	v_mul_f32_e32 v135, 0x42000000, v68
	v_mul_f32_e32 v136, 0x42000000, v72
	v_mov_b32_e32 v134, v141
	v_cvt_pk_fp8_f32 v134, v135, v136
	v_mul_f32_e32 v137, 0x42000000, v76
	v_mul_f32_e32 v138, 0x42000000, v80
	v_mul_f32_e32 v136, 0x42000000, v84
	v_cvt_pk_fp8_f32 v134, v137, v138 op_sel:[0,0,1]
	v_mul_f32_e32 v137, 0x42000000, v88
	v_mov_b32_e32 v135, v141
	v_cvt_pk_fp8_f32 v135, v136, v137
	v_mul_f32_e32 v138, 0x42000000, v92
	v_mul_f32_e32 v139, 0x42000000, v96
	v_mul_f32_e32 v137, 0x42000000, v100
	v_cvt_pk_fp8_f32 v135, v138, v139 op_sel:[0,0,1]
	v_mul_f32_e32 v138, 0x42000000, v104
	v_mov_b32_e32 v136, v141
	v_cvt_pk_fp8_f32 v136, v137, v138
	v_mul_f32_e32 v139, 0x42000000, v108
	v_mul_f32_e32 v152, 0x42000000, v112
	v_mul_f32_e32 v138, 0x42000000, v116
	v_cvt_pk_fp8_f32 v136, v139, v152 op_sel:[0,0,1]
	v_mul_f32_e32 v139, 0x42000000, v120
	v_mov_b32_e32 v137, v141
	v_cvt_pk_fp8_f32 v137, v138, v139
	v_mul_f32_e32 v152, 0x42000000, v124
	v_mul_f32_e32 v202, 0x42000000, v128
	s_and_b32 s2, s30, 0x780
	v_cvt_pk_fp8_f32 v137, v152, v202 op_sel:[0,0,1]
	s_mov_b32 s3, s79
	v_lshl_add_u64 v[132:133], v[132:133], 0, s[2:3]
	v_lshl_add_u64 v[132:133], v[132:133], 0, v[146:147]
	global_store_dwordx4 v[132:133], v[134:137], off nt
	v_mul_f32_e32 v138, 0x42000000, v81
	v_mul_f32_e32 v139, 0x42000000, v97
	v_mul_f32_e32 v135, 0x42000000, v69
	v_mul_f32_e32 v136, 0x42000000, v73
	v_mov_b32_e32 v134, v141
	v_cvt_pk_fp8_f32 v134, v135, v136
	v_mul_f32_e32 v137, 0x42000000, v77
	v_mul_f32_e32 v136, 0x42000000, v85
	v_mov_b32_e32 v135, v141
	v_cvt_pk_fp8_f32 v134, v137, v138 op_sel:[0,0,1]
	v_mul_f32_e32 v137, 0x42000000, v89
	v_cvt_pk_fp8_f32 v135, v136, v137
	v_mul_f32_e32 v138, 0x42000000, v93
	v_mul_f32_e32 v137, 0x42000000, v101
	v_mov_b32_e32 v136, v141
	v_cvt_pk_fp8_f32 v135, v138, v139 op_sel:[0,0,1]
	v_mul_f32_e32 v138, 0x42000000, v105
	v_cvt_pk_fp8_f32 v136, v137, v138
	v_mul_f32_e32 v139, 0x42000000, v109
	v_mul_f32_e32 v152, 0x42000000, v113
	v_mul_f32_e32 v138, 0x42000000, v117
	v_cvt_pk_fp8_f32 v136, v139, v152 op_sel:[0,0,1]
	v_mul_f32_e32 v139, 0x42000000, v121
	v_mov_b32_e32 v137, v141
	v_cvt_pk_fp8_f32 v137, v138, v139
	v_mul_f32_e32 v152, 0x42000000, v125
	v_mul_f32_e32 v202, 0x42000000, v129
	v_mul_f32_e32 v138, 0x42000000, v82
	v_cvt_pk_fp8_f32 v137, v152, v202 op_sel:[0,0,1]
	v_mul_f32_e32 v139, 0x42000000, v98
	v_mul_f32_e32 v152, 0x42000000, v114
	v_mul_f32_e32 v202, 0x42000000, v130
	global_store_dwordx4 v[132:133], v[134:137], off offset:2048 nt
	s_nop 1
	v_mul_f32_e32 v135, 0x42000000, v70
	v_mul_f32_e32 v136, 0x42000000, v74
	v_mov_b32_e32 v134, v141
	v_cvt_pk_fp8_f32 v134, v135, v136
	v_mul_f32_e32 v137, 0x42000000, v78
	v_mul_f32_e32 v136, 0x42000000, v86
	v_mov_b32_e32 v135, v141
	v_cvt_pk_fp8_f32 v134, v137, v138 op_sel:[0,0,1]
	v_mul_f32_e32 v137, 0x42000000, v90
	v_cvt_pk_fp8_f32 v135, v136, v137
	v_mul_f32_e32 v138, 0x42000000, v94
	v_mul_f32_e32 v137, 0x42000000, v102
	v_mov_b32_e32 v136, v141
	v_cvt_pk_fp8_f32 v135, v138, v139 op_sel:[0,0,1]
	v_mul_f32_e32 v138, 0x42000000, v106
	v_cvt_pk_fp8_f32 v136, v137, v138
	v_mul_f32_e32 v139, 0x42000000, v110
	v_mul_f32_e32 v138, 0x42000000, v118
	v_mov_b32_e32 v137, v141
	v_cvt_pk_fp8_f32 v136, v139, v152 op_sel:[0,0,1]
	v_mul_f32_e32 v139, 0x42000000, v122
	v_cvt_pk_fp8_f32 v137, v138, v139
	v_mul_f32_e32 v152, 0x42000000, v126
	v_add_co_u32_e32 v138, vcc, s91, v132
	v_cvt_pk_fp8_f32 v137, v152, v202 op_sel:[0,0,1]
	s_nop 0
	v_addc_co_u32_e32 v139, vcc, 0, v133, vcc
	v_mul_f32_e32 v133, 0x42000000, v71
	global_store_dwordx4 v[138:139], v[134:137], off nt
	v_mov_b32_e32 v132, v141
	v_mul_f32_e32 v152, 0x42000000, v115
	v_mul_f32_e32 v134, 0x42000000, v75
	v_cvt_pk_fp8_f32 v132, v133, v134
	v_mul_f32_e32 v135, 0x42000000, v79
	v_mul_f32_e32 v136, 0x42000000, v83
	v_mul_f32_e32 v134, 0x42000000, v87
	v_cvt_pk_fp8_f32 v132, v135, v136 op_sel:[0,0,1]
	v_mul_f32_e32 v135, 0x42000000, v91
	v_mov_b32_e32 v133, v141
	v_cvt_pk_fp8_f32 v133, v134, v135
	v_mul_f32_e32 v136, 0x42000000, v95
	v_mul_f32_e32 v137, 0x42000000, v99
	v_mul_f32_e32 v135, 0x42000000, v103
	v_cvt_pk_fp8_f32 v133, v136, v137 op_sel:[0,0,1]
	v_mul_f32_e32 v136, 0x42000000, v107
	v_mov_b32_e32 v134, v141
	v_cvt_pk_fp8_f32 v134, v135, v136
	v_mul_f32_e32 v137, 0x42000000, v111
	v_mul_f32_e32 v136, 0x42000000, v119
	v_mov_b32_e32 v135, v141
	v_cvt_pk_fp8_f32 v134, v137, v152 op_sel:[0,0,1]
	v_mul_f32_e32 v137, 0x42000000, v123
	v_cvt_pk_fp8_f32 v135, v136, v137
	v_mul_f32_e32 v152, 0x42000000, v127
	v_mul_f32_e32 v202, 0x42000000, v131
	v_cvt_pk_fp8_f32 v135, v152, v202 op_sel:[0,0,1]
	global_store_dwordx4 v[138:139], v[132:135], off offset:2048 nt

.LBB0_607:
	s_waitcnt vmcnt(15)
	v_mul_f32_e32 v135, 0x42000000, v68
	s_waitcnt vmcnt(14)
	v_mul_f32_e32 v136, 0x42000000, v72
	v_mov_b32_e32 v134, v141
	v_cvt_pk_fp8_f32 v134, v135, v136
	s_waitcnt vmcnt(13)
	v_mul_f32_e32 v137, 0x42000000, v76
	s_waitcnt vmcnt(12)
	v_mul_f32_e32 v138, 0x42000000, v80
	s_waitcnt vmcnt(11)
	v_mul_f32_e32 v136, 0x42000000, v84
	v_cvt_pk_fp8_f32 v134, v137, v138 op_sel:[0,0,1]
	s_waitcnt vmcnt(10)
	v_mul_f32_e32 v137, 0x42000000, v88
	v_mov_b32_e32 v135, v141
	v_cvt_pk_fp8_f32 v135, v136, v137
	s_waitcnt vmcnt(9)
	v_mul_f32_e32 v138, 0x42000000, v92
	s_waitcnt vmcnt(8)
	v_mul_f32_e32 v139, 0x42000000, v96
	s_waitcnt vmcnt(7)
	v_mul_f32_e32 v137, 0x42000000, v100
	v_cvt_pk_fp8_f32 v135, v138, v139 op_sel:[0,0,1]
	s_waitcnt vmcnt(6)
	v_mul_f32_e32 v138, 0x42000000, v104
	v_mov_b32_e32 v136, v141
	v_cvt_pk_fp8_f32 v136, v137, v138
	s_waitcnt vmcnt(5)
	v_mul_f32_e32 v139, 0x42000000, v108
	s_waitcnt vmcnt(4)
	v_mul_f32_e32 v152, 0x42000000, v112
	s_waitcnt vmcnt(3)
	v_mul_f32_e32 v138, 0x42000000, v116
	v_cvt_pk_fp8_f32 v136, v139, v152 op_sel:[0,0,1]
	s_waitcnt vmcnt(2)
	v_mul_f32_e32 v139, 0x42000000, v120
	v_mov_b32_e32 v137, v141
	v_cvt_pk_fp8_f32 v137, v138, v139
	s_waitcnt vmcnt(1)
	v_mul_f32_e32 v152, 0x42000000, v124
	s_waitcnt vmcnt(0)
	v_mul_f32_e32 v202, 0x42000000, v128
	s_and_b32 s2, s30, 0x780
	v_cvt_pk_fp8_f32 v137, v152, v202 op_sel:[0,0,1]
	s_mov_b32 s3, s79
	v_lshl_add_u64 v[132:133], v[132:133], 0, s[2:3]
	v_lshl_add_u64 v[132:133], v[132:133], 0, v[146:147]
	global_store_dwordx4 v[132:133], v[134:137], off nt
	v_mul_f32_e32 v138, 0x42000000, v81
	v_mul_f32_e32 v139, 0x42000000, v97
	v_mul_f32_e32 v135, 0x42000000, v69
	v_mul_f32_e32 v136, 0x42000000, v73
	v_mov_b32_e32 v134, v141
	v_cvt_pk_fp8_f32 v134, v135, v136
	v_mul_f32_e32 v137, 0x42000000, v77
	v_mul_f32_e32 v136, 0x42000000, v85
	v_mov_b32_e32 v135, v141
	v_cvt_pk_fp8_f32 v134, v137, v138 op_sel:[0,0,1]
	v_mul_f32_e32 v137, 0x42000000, v89
	v_cvt_pk_fp8_f32 v135, v136, v137
	v_mul_f32_e32 v138, 0x42000000, v93
	v_mul_f32_e32 v137, 0x42000000, v101
	v_mov_b32_e32 v136, v141
	v_cvt_pk_fp8_f32 v135, v138, v139 op_sel:[0,0,1]
	v_mul_f32_e32 v138, 0x42000000, v105
	v_cvt_pk_fp8_f32 v136, v137, v138
	v_mul_f32_e32 v139, 0x42000000, v109
	v_mul_f32_e32 v152, 0x42000000, v113
	v_mul_f32_e32 v138, 0x42000000, v117
	v_cvt_pk_fp8_f32 v136, v139, v152 op_sel:[0,0,1]
	v_mul_f32_e32 v139, 0x42000000, v121
	v_mov_b32_e32 v137, v141
	v_cvt_pk_fp8_f32 v137, v138, v139
	v_mul_f32_e32 v152, 0x42000000, v125
	v_mul_f32_e32 v202, 0x42000000, v129
	v_mul_f32_e32 v138, 0x42000000, v82
	v_cvt_pk_fp8_f32 v137, v152, v202 op_sel:[0,0,1]
	v_mul_f32_e32 v139, 0x42000000, v98
	v_mul_f32_e32 v152, 0x42000000, v114
	v_mul_f32_e32 v202, 0x42000000, v130
	global_store_dwordx4 v[132:133], v[134:137], off offset:2048 nt
	s_nop 1
	v_mul_f32_e32 v135, 0x42000000, v70
	v_mul_f32_e32 v136, 0x42000000, v74
	v_mov_b32_e32 v134, v141
	v_cvt_pk_fp8_f32 v134, v135, v136
	v_mul_f32_e32 v137, 0x42000000, v78
	v_mul_f32_e32 v136, 0x42000000, v86
	v_mov_b32_e32 v135, v141
	v_cvt_pk_fp8_f32 v134, v137, v138 op_sel:[0,0,1]
	v_mul_f32_e32 v137, 0x42000000, v90
	v_cvt_pk_fp8_f32 v135, v136, v137
	v_mul_f32_e32 v138, 0x42000000, v94
	v_mul_f32_e32 v137, 0x42000000, v102
	v_mov_b32_e32 v136, v141
	v_cvt_pk_fp8_f32 v135, v138, v139 op_sel:[0,0,1]
	v_mul_f32_e32 v138, 0x42000000, v106
	v_cvt_pk_fp8_f32 v136, v137, v138
	v_mul_f32_e32 v139, 0x42000000, v110
	v_mul_f32_e32 v138, 0x42000000, v118
	v_mov_b32_e32 v137, v141
	v_cvt_pk_fp8_f32 v136, v139, v152 op_sel:[0,0,1]
	v_mul_f32_e32 v139, 0x42000000, v122
	v_cvt_pk_fp8_f32 v137, v138, v139
	v_mul_f32_e32 v152, 0x42000000, v126
	v_add_co_u32_e32 v138, vcc, s91, v132
	v_cvt_pk_fp8_f32 v137, v152, v202 op_sel:[0,0,1]
	s_nop 0
	v_addc_co_u32_e32 v139, vcc, 0, v133, vcc
	v_mul_f32_e32 v133, 0x42000000, v71
	global_store_dwordx4 v[138:139], v[134:137], off nt
	v_mov_b32_e32 v132, v141
	v_mul_f32_e32 v152, 0x42000000, v115
	v_mul_f32_e32 v134, 0x42000000, v75
	v_cvt_pk_fp8_f32 v132, v133, v134
	v_mul_f32_e32 v135, 0x42000000, v79
	v_mul_f32_e32 v136, 0x42000000, v83
	v_mul_f32_e32 v134, 0x42000000, v87
	v_cvt_pk_fp8_f32 v132, v135, v136 op_sel:[0,0,1]
	v_mul_f32_e32 v135, 0x42000000, v91
	v_mov_b32_e32 v133, v141
	v_cvt_pk_fp8_f32 v133, v134, v135
	v_mul_f32_e32 v136, 0x42000000, v95
	v_mul_f32_e32 v137, 0x42000000, v99
	v_mul_f32_e32 v135, 0x42000000, v103
	v_cvt_pk_fp8_f32 v133, v136, v137 op_sel:[0,0,1]
	v_mul_f32_e32 v136, 0x42000000, v107
	v_mov_b32_e32 v134, v141
	v_cvt_pk_fp8_f32 v134, v135, v136
	v_mul_f32_e32 v137, 0x42000000, v111
	v_mul_f32_e32 v136, 0x42000000, v119
	v_mov_b32_e32 v135, v141
	v_cvt_pk_fp8_f32 v134, v137, v152 op_sel:[0,0,1]
	v_mul_f32_e32 v137, 0x42000000, v123
	v_cvt_pk_fp8_f32 v135, v136, v137
	v_mul_f32_e32 v152, 0x42000000, v127
	v_mul_f32_e32 v202, 0x42000000, v131
	v_cvt_pk_fp8_f32 v135, v152, v202 op_sel:[0,0,1]
	global_store_dwordx4 v[138:139], v[132:135], off offset:2048 nt

; __global__ void __launch_bounds__(NTHREADS, 2) fwd(Args args) {
;     ...
;                 f32x4 cv[16];
; #pragma unroll 1
;                 while (cvs.t < ml::T_CONV) { CV_ISSUE(); CV_FINISH(); }
.LBB0_626:
	s_waitcnt vmcnt(0)
	v_mul_f32_e32 v12, 0x42000000, v12
	v_mul_f32_e32 v8, 0x42000000, v8
	v_mov_b32_e32 v77, 0
	v_cvt_pk_fp8_f32 v77, v12, v8
	v_mul_f32_e32 v4, 0x42000000, v4
	v_mul_f32_e32 v0, 0x42000000, v0
	v_mov_b32_e32 v78, 0
	v_cvt_pk_fp8_f32 v77, v4, v0 op_sel:[0,0,1]
	v_mul_f32_e32 v0, 0x42000000, v61
	v_mul_f32_e32 v4, 0x42000000, v57
	v_cvt_pk_fp8_f32 v78, v0, v4
	v_mul_f32_e32 v0, 0x42000000, v45
	v_mul_f32_e32 v4, 0x42000000, v41
	v_mov_b32_e32 v79, 0
	v_cvt_pk_fp8_f32 v79, v0, v4
	v_mul_f32_e32 v0, 0x42000000, v37
	v_mul_f32_e32 v4, 0x42000000, v33
	v_mov_b32_e32 v80, 0
	v_cvt_pk_fp8_f32 v79, v0, v4 op_sel:[0,0,1]
	v_mul_f32_e32 v0, 0x42000000, v29
	v_mul_f32_e32 v4, 0x42000000, v25
	v_cvt_pk_fp8_f32 v80, v0, v4
	v_mul_f32_e32 v0, 0x42000000, v13
	v_mul_f32_e32 v4, 0x42000000, v9
	v_mov_b32_e32 v81, 0
	v_cvt_pk_fp8_f32 v81, v0, v4
	v_mul_f32_e32 v60, 0x42000000, v60
	v_mul_f32_e32 v56, 0x42000000, v56
	v_mov_b32_e32 v74, 0
	v_mul_f32_e32 v44, 0x42000000, v44
	v_mul_f32_e32 v40, 0x42000000, v40
	v_mov_b32_e32 v75, 0
	v_mul_f32_e32 v28, 0x42000000, v28
	v_mul_f32_e32 v24, 0x42000000, v24
	v_mov_b32_e32 v76, 0
	v_cvt_pk_fp8_f32 v74, v60, v56
	v_cvt_pk_fp8_f32 v75, v44, v40
	v_cvt_pk_fp8_f32 v76, v28, v24
	s_and_b32 s2, s2, 0x780
	v_mul_f32_e32 v0, 0x42000000, v5
	v_mul_f32_e32 v1, 0x42000000, v1
	v_cvt_pk_fp8_f32 v81, v0, v1 op_sel:[0,0,1]
	v_lshl_add_u64 v[0:1], v[72:73], 0, s[2:3]
	v_mul_f32_e32 v4, 0x42000000, v62
	v_mul_f32_e32 v5, 0x42000000, v58
	v_mov_b32_e32 v72, 0
	v_mul_f32_e32 v52, 0x42000000, v52
	v_mul_f32_e32 v48, 0x42000000, v48
	v_mul_f32_e32 v36, 0x42000000, v36
	v_mul_f32_e32 v32, 0x42000000, v32
	v_mul_f32_e32 v20, 0x42000000, v20
	v_mul_f32_e32 v16, 0x42000000, v16
	v_mul_f32_e32 v8, 0x42000000, v53
	v_mul_f32_e32 v12, 0x42000000, v49
	v_cvt_pk_fp8_f32 v72, v4, v5
	v_mul_f32_e32 v4, 0x42000000, v46
	v_mul_f32_e32 v5, 0x42000000, v42
	v_mov_b32_e32 v73, 0
	v_cvt_pk_fp8_f32 v74, v52, v48 op_sel:[0,0,1]
	v_cvt_pk_fp8_f32 v75, v36, v32 op_sel:[0,0,1]
	v_cvt_pk_fp8_f32 v76, v20, v16 op_sel:[0,0,1]
	v_cvt_pk_fp8_f32 v78, v8, v12 op_sel:[0,0,1]
	v_mul_f32_e32 v8, 0x42000000, v21
	v_mul_f32_e32 v12, 0x42000000, v17
	v_cvt_pk_fp8_f32 v73, v4, v5
	v_cvt_pk_fp8_f32 v80, v8, v12 op_sel:[0,0,1]
	v_lshl_add_u64 v[0:1], v[0:1], 0, v[64:65]
	v_mul_f32_e32 v4, 0x42000000, v38
	v_mul_f32_e32 v5, 0x42000000, v34
	global_store_dwordx4 v[0:1], v[74:77], off nt
	global_store_dwordx4 v[0:1], v[78:81], off offset:2048 nt
	v_cvt_pk_fp8_f32 v73, v4, v5 op_sel:[0,0,1]
	v_mul_f32_e32 v4, 0x42000000, v30
	v_mul_f32_e32 v5, 0x42000000, v26
	v_mov_b32_e32 v74, 0
	v_cvt_pk_fp8_f32 v74, v4, v5
	v_mul_f32_e32 v4, 0x42000000, v14
	v_mul_f32_e32 v5, 0x42000000, v10
	v_mov_b32_e32 v75, 0
	v_cvt_pk_fp8_f32 v75, v4, v5
	v_mul_f32_e32 v8, 0x42000000, v54
	v_mul_f32_e32 v9, 0x42000000, v50
	v_cvt_pk_fp8_f32 v72, v8, v9 op_sel:[0,0,1]
	v_mul_f32_e32 v8, 0x42000000, v22
	v_mul_f32_e32 v9, 0x42000000, v18
	v_mul_f32_e32 v4, 0x42000000, v6
	v_mul_f32_e32 v2, 0x42000000, v2
	v_cvt_pk_fp8_f32 v74, v8, v9 op_sel:[0,0,1]
	v_cvt_pk_fp8_f32 v75, v4, v2 op_sel:[0,0,1]
	v_mul_f32_e32 v2, 0x42000000, v63
	v_mul_f32_e32 v4, 0x42000000, v59
	v_mov_b32_e32 v8, 0
	v_cvt_pk_fp8_f32 v8, v2, v4
	v_mul_f32_e32 v2, 0x42000000, v47
	v_mul_f32_e32 v4, 0x42000000, v43
	v_mov_b32_e32 v9, 0
	v_cvt_pk_fp8_f32 v9, v2, v4
	v_mul_f32_e32 v2, 0x42000000, v39
	v_mul_f32_e32 v4, 0x42000000, v35
	v_mov_b32_e32 v10, 0
	v_cvt_pk_fp8_f32 v9, v2, v4 op_sel:[0,0,1]
	v_mul_f32_e32 v2, 0x42000000, v31
	v_mul_f32_e32 v4, 0x42000000, v27
	v_cvt_pk_fp8_f32 v10, v2, v4
	v_mul_f32_e32 v2, 0x42000000, v15
	v_mul_f32_e32 v4, 0x42000000, v11
	v_mov_b32_e32 v11, 0
	v_cvt_pk_fp8_f32 v11, v2, v4
	v_mul_f32_e32 v5, 0x42000000, v55
	v_mul_f32_e32 v6, 0x42000000, v51
	v_cvt_pk_fp8_f32 v8, v5, v6 op_sel:[0,0,1]
	v_mul_f32_e32 v5, 0x42000000, v23
	v_mul_f32_e32 v6, 0x42000000, v19
	v_mul_f32_e32 v2, 0x42000000, v7
	v_mul_f32_e32 v3, 0x42000000, v3
	v_cvt_pk_fp8_f32 v10, v5, v6 op_sel:[0,0,1]
	v_cvt_pk_fp8_f32 v11, v2, v3 op_sel:[0,0,1]
	s_movk_i32 s2, 0x1000
	v_add_co_u32_e32 v0, vcc, s2, v0
	s_add_i32 s33, s33, s62
	s_add_i32 s0, s0, s1
	s_add_i32 s36, s36, s37
	s_add_i32 s38, s38, s39
	v_addc_co_u32_e32 v1, vcc, 0, v1, vcc
	s_cmp_lt_i32 s33, 0x18000
	global_store_dwordx4 v[0:1], v[72:75], off nt
	global_store_dwordx4 v[0:1], v[8:11], off offset:2048 nt
	s_cbranch_scc0 .LBB0_636
